# P11: uniform loop test branches on SCC directly; 15 dead upper-half inits before cvt_pk_fp8 removed from the query epilogue
# baseline (speedup 1.0000x reference)
.LBB0_1463:
	s_waitcnt lgkmcnt(0)
	v_lshlrev_b32_e32 v0, 6, v197
	v_and_b32_e32 v0, 0x3fc0, v0
	v_add_u32_e32 v0, v189, v0
	v_bfe_u32 v114, v197, 8, 8
	v_bfe_u32 v115, v197, 16, 8
	v_lshrrev_b32_e32 v116, 24, v197
	ds_read_b32 v220, v198
	v_lshl_add_u32 v114, v114, 6, v189
	v_lshl_add_u32 v115, v115, 6, v189
	v_lshl_add_u32 v116, v116, 6, v189
	ds_read_b32 v0, v0
	ds_read_b32 v201, v114
	ds_read_b32 v202, v115
	ds_read_b32 v203, v116
	s_waitcnt vmcnt(7)
	v_cvt_scalef32_pk_bf16_fp8 v114, v110, 1.0
	v_cvt_scalef32_pk_bf16_fp8 v115, v110, 1.0 op_sel:[1,0,0]
	v_cvt_scalef32_pk_bf16_fp8 v116, v111, 1.0
	v_cvt_scalef32_pk_bf16_fp8 v117, v111, 1.0 op_sel:[1,0,0]
	v_cvt_scalef32_pk_bf16_fp8 v118, v112, 1.0
	v_cvt_scalef32_pk_bf16_fp8 v119, v112, 1.0 op_sel:[1,0,0]
	v_cvt_scalef32_pk_bf16_fp8 v120, v113, 1.0
	v_cvt_scalef32_pk_bf16_fp8 v121, v113, 1.0 op_sel:[1,0,0]
	s_waitcnt vmcnt(6)
	v_cvt_scalef32_pk_bf16_fp8 v122, v106, 1.0
	v_cvt_scalef32_pk_bf16_fp8 v123, v106, 1.0 op_sel:[1,0,0]
	v_cvt_scalef32_pk_bf16_fp8 v124, v107, 1.0
	v_cvt_scalef32_pk_bf16_fp8 v125, v107, 1.0 op_sel:[1,0,0]
	v_cvt_scalef32_pk_bf16_fp8 v126, v108, 1.0
	v_cvt_scalef32_pk_bf16_fp8 v127, v108, 1.0 op_sel:[1,0,0]
	v_cvt_scalef32_pk_bf16_fp8 v128, v109, 1.0
	v_cvt_scalef32_pk_bf16_fp8 v129, v109, 1.0 op_sel:[1,0,0]
	s_waitcnt vmcnt(5)
	v_cvt_scalef32_pk_bf16_fp8 v146, v102, 1.0
	v_cvt_scalef32_pk_bf16_fp8 v147, v102, 1.0 op_sel:[1,0,0]
	v_cvt_scalef32_pk_bf16_fp8 v148, v103, 1.0
	v_cvt_scalef32_pk_bf16_fp8 v149, v103, 1.0 op_sel:[1,0,0]
	v_cvt_scalef32_pk_bf16_fp8 v150, v104, 1.0
	v_cvt_scalef32_pk_bf16_fp8 v151, v104, 1.0 op_sel:[1,0,0]
	v_cvt_scalef32_pk_bf16_fp8 v152, v105, 1.0
	v_cvt_scalef32_pk_bf16_fp8 v153, v105, 1.0 op_sel:[1,0,0]
	s_waitcnt vmcnt(4)
	v_cvt_scalef32_pk_bf16_fp8 v204, v98, 1.0
	v_cvt_scalef32_pk_bf16_fp8 v205, v98, 1.0 op_sel:[1,0,0]
	v_cvt_scalef32_pk_bf16_fp8 v206, v99, 1.0
	v_cvt_scalef32_pk_bf16_fp8 v207, v99, 1.0 op_sel:[1,0,0]
	v_cvt_scalef32_pk_bf16_fp8 v208, v100, 1.0
	v_cvt_scalef32_pk_bf16_fp8 v209, v100, 1.0 op_sel:[1,0,0]
	v_cvt_scalef32_pk_bf16_fp8 v210, v101, 1.0
	v_cvt_scalef32_pk_bf16_fp8 v211, v101, 1.0 op_sel:[1,0,0]
	v_and_b32_e32 v98, 0xffff, v196
	v_mov_b32_e32 v99, s7
	v_lshl_add_u64 v[98:99], s[18:19], 0, v[98:99]
	v_lshlrev_b64 v[98:99], 8, v[98:99]
	v_lshl_add_u64 v[98:99], v[156:157], 0, v[98:99]
	global_load_dwordx4 v[110:113], v[98:99], off
	global_load_dwordx4 v[106:109], v[98:99], off offset:64
	global_load_dwordx4 v[102:105], v[98:99], off offset:128
	s_nop 0
	global_load_dwordx4 v[98:101], v[98:99], off offset:192
	v_mfma_f32_16x16x32_bf16 v[212:215], v[114:117], v[66:69], 0
	v_add_u32_e32 v196, -16, v199
	v_cmp_ge_i32_e32 vcc, s6, v196
	v_mfma_f32_16x16x32_bf16 v[212:215], v[122:125], v[70:73], v[212:215]
	s_nop 0
	v_cndmask_b32_e32 v196, 0, v196, vcc
	v_lshl_add_u32 v196, v196, 1, s30
	ds_read_u16 v196, v196
	v_mfma_f32_16x16x32_bf16 v[216:219], v[118:121], v[82:85], 0
	ds_write_b128 v193, v[114:117]
	ds_write_b128 v194, v[118:121]
	ds_write_b128 v190, v[122:125]
	ds_write_b128 v191, v[126:129]
	ds_write_b128 v192, v[146:149]
	ds_write_b128 v186, v[150:153]
	ds_write_b128 v187, v[204:207]
	ds_write_b128 v188, v[208:211]
	v_mfma_f32_16x16x32_bf16 v[114:117], v[146:149], v[74:77], v[212:215]
	ds_read_b32 v197, v198 offset:16
	v_mfma_f32_16x16x32_bf16 v[216:219], v[126:129], v[86:89], v[216:219]
	v_mfma_f32_16x16x32_bf16 v[146:149], v[204:207], v[78:81], v[114:117]
	s_waitcnt lgkmcnt(14)
	s_nop 3
	v_lshlrev_b32_e32 v114, 6, v220
	v_and_b32_e32 v114, 0x3fc0, v114
	v_mfma_f32_16x16x32_bf16 v[118:121], v[150:153], v[90:93], v[216:219]
	v_add_u32_e32 v114, v189, v114
	v_bfe_u32 v115, v220, 8, 8
	v_bfe_u32 v116, v220, 16, 8
	v_lshrrev_b32_e32 v117, 24, v220
	v_lshl_add_u32 v115, v115, 6, v189
	v_lshl_add_u32 v116, v116, 6, v189
	v_lshl_add_u32 v117, v117, 6, v189
	ds_read_b32 v204, v114
	ds_read_b32 v205, v115
	ds_read_b32 v206, v116
	ds_read_b32 v207, v117
	v_mfma_f32_16x16x32_bf16 v[150:153], v[208:211], v[94:97], v[118:121]
	s_waitcnt lgkmcnt(13)
	v_and_b32_e32 v248, 0xffff, v196
	v_mov_b32_e32 v249, s7
	v_lshl_add_u64 v[248:249], s[18:19], 0, v[248:249]
	v_lshlrev_b64 v[248:249], 8, v[248:249]
	v_lshl_add_u64 v[248:249], v[156:157], 0, v[248:249]
	s_cmp_gt_u32 s17, 11
	s_cselect_b64 s[20:21], -1, 0
	s_cbranch_scc1 .LBB0_1465
	v_cmp_ge_i32_e32 vcc, s6, v199
	s_nop 1
	v_cndmask_b32_e32 v196, 0, v199, vcc
	v_lshl_add_u32 v196, v196, 1, s30
	ds_read_u16 v196, v196

.LBB0_1471:
	v_sub_f32_e32 v71, v101, v70
	v_sub_f32_e32 v72, v100, v70
	v_sub_f32_e32 v73, v99, v70
	v_sub_f32_e32 v74, v98, v70
	v_exp_f32_e32 v71, v71
	v_exp_f32_e32 v72, v72
	v_exp_f32_e32 v73, v73
	v_exp_f32_e32 v74, v74
	v_sub_f32_e32 v69, v69, v70
	v_sub_f32_e32 v68, v68, v70
	v_sub_f32_e32 v67, v67, v70
	v_sub_f32_e32 v66, v66, v70
	v_exp_f32_e32 v69, v69
	v_exp_f32_e32 v68, v68
	v_exp_f32_e32 v77, v67
	v_exp_f32_e32 v70, v66
	v_add_f32_e32 v75, v71, v72
	v_add_f32_e32 v76, v73, v74
	v_add_f32_e32 v66, v75, v76
	v_fmac_f32_e32 v66, v185, v0
	v_add_f32_e32 v0, v69, v68
	v_add_f32_e32 v67, v77, v70
	v_add_f32_e32 v0, v0, v67
	v_add_f32_e32 v0, v0, v66
	v_cvt_pk_bf16_f32 v66, v71, v72
	v_cvt_pk_bf16_f32 v68, v69, v68
	v_cvt_pk_bf16_f32 v69, v77, v70
	ds_read_b64_tr_b16 v[70:71],v177
	v_cvt_pk_bf16_f32 v67, v73, v74
	ds_read_b64_tr_b16 v[72:73],v177 offset:8192
	ds_read_b64_tr_b16 v[74:75],v178
	ds_read_b64_tr_b16 v[76:77],v178 offset:8192
	ds_read_b64_tr_b16 v[78:79],v179
	ds_read_b64_tr_b16 v[80:81],v179 offset:8192
	ds_read_b64_tr_b16 v[82:83],v180
	ds_read_b64_tr_b16 v[84:85],v180 offset:8192
	ds_read_b64_tr_b16 v[86:87],v181
	ds_read_b64_tr_b16 v[88:89],v181 offset:8192
	ds_read_b64_tr_b16 v[90:91],v182
	ds_read_b64_tr_b16 v[92:93],v182 offset:8192
	ds_read_b64_tr_b16 v[94:95],v183
	ds_read_b64_tr_b16 v[96:97],v183 offset:8192
	ds_read_b64_tr_b16 v[98:99],v184
	ds_read_b64_tr_b16 v[100:101],v184 offset:8192
	s_waitcnt lgkmcnt(0)
	s_nop 1
	v_mfma_f32_16x16x32_bf16 v[62:65], v[66:69], v[70:73], v[62:65]
	ds_read_b64_tr_b16 v[70:71],v175
	ds_read_b64_tr_b16 v[72:73],v175 offset:8192
	v_mfma_f32_16x16x32_bf16 v[58:61], v[66:69], v[74:77], v[58:61]
	ds_read_b64_tr_b16 v[74:75],v176
	ds_read_b64_tr_b16 v[76:77],v176 offset:8192
	v_mfma_f32_16x16x32_bf16 v[54:57], v[66:69], v[78:81], v[54:57]
	ds_read_b64_tr_b16 v[78:79],v174
	ds_read_b64_tr_b16 v[80:81],v174 offset:8192
	v_mfma_f32_16x16x32_bf16 v[50:53], v[66:69], v[82:85], v[50:53]
	ds_read_b64_tr_b16 v[82:83],v172
	ds_read_b64_tr_b16 v[84:85],v172 offset:8192
	v_mfma_f32_16x16x32_bf16 v[46:49], v[66:69], v[86:89], v[46:49]
	ds_read_b64_tr_b16 v[86:87],v173
	ds_read_b64_tr_b16 v[88:89],v173 offset:8192
	v_mfma_f32_16x16x32_bf16 v[42:45], v[66:69], v[90:93], v[42:45]
	ds_read_b64_tr_b16 v[90:91],v171
	ds_read_b64_tr_b16 v[92:93],v171 offset:8192
	ds_read_b64_tr_b16 v[102:103],v169
	ds_read_b64_tr_b16 v[104:105],v169 offset:8192
	v_mfma_f32_16x16x32_bf16 v[38:41], v[66:69], v[94:97], v[38:41]
	ds_read_b64_tr_b16 v[94:95],v170
	ds_read_b64_tr_b16 v[96:97],v170 offset:8192
	s_waitcnt lgkmcnt(0)
	v_mfma_f32_16x16x32_bf16 v[34:37], v[66:69], v[98:101], v[34:37]
	v_mfma_f32_16x16x32_bf16 v[30:33], v[66:69], v[70:73], v[30:33]
	ds_bpermute_b32 v70, v160, v0
	s_waitcnt lgkmcnt(0)
	s_add_u32 s2, s26, s2
	v_mfma_f32_16x16x32_bf16 v[26:29], v[66:69], v[74:77], v[26:29]
	s_addc_u32 s3, s27, s3
	s_waitcnt lgkmcnt(0)
	v_add_f32_e32 v0, v0, v70
	ds_bpermute_b32 v70, v161, v0
	v_mfma_f32_16x16x32_bf16 v[22:25], v[66:69], v[78:81], v[22:25]
	s_lshl_b32 s17, s15, 1
	s_lshl_b32 s44, s15, 5
	s_mov_b32 s45, -1
	s_waitcnt lgkmcnt(0)
	v_add_f32_e32 v0, v0, v70
	v_div_scale_f32 v70, s[18:19], v0, v0, 1.0
	v_rcp_f32_e32 v71, v70
	v_div_scale_f32 v72, vcc, 1.0, v0, 1.0
	v_mfma_f32_16x16x32_bf16 v[18:21], v[66:69], v[82:85], v[18:21]
	v_fma_f32 v73, -v70, v71, 1.0
	v_fmac_f32_e32 v71, v73, v71
	v_mul_f32_e32 v73, v72, v71
	v_fma_f32 v74, -v70, v73, v72
	v_fmac_f32_e32 v73, v74, v71
	v_fma_f32 v70, -v70, v73, v72
	v_div_fmas_f32 v70, v70, v71, v73
	v_div_fixup_f32 v0, v70, v0, 1.0
	ds_bpermute_b32 v71, v168, v0
	ds_bpermute_b32 v72, v165, v0
	ds_bpermute_b32 v70, v167, v0
	ds_bpermute_b32 v0, v166, v0
	v_mfma_f32_16x16x32_bf16 v[14:17], v[66:69], v[86:89], v[14:17]
	s_waitcnt lgkmcnt(3)
	v_mul_f32_e32 v63, v63, v71
	v_med3_f32 v63, v63, s39, v162
	s_waitcnt lgkmcnt(1)
	v_mul_f32_e32 v58, v58, v70
	v_mfma_f32_16x16x32_bf16 v[10:13], v[66:69], v[90:93], v[10:13]
	v_med3_f32 v58, v58, s39, v162
	v_mul_f32_e32 v54, v54, v70
	v_med3_f32 v54, v54, s39, v162
	v_mfma_f32_16x16x32_bf16 v[6:9], v[66:69], v[102:105], v[6:9]
	v_mul_f32_e32 v50, v50, v70
	v_med3_f32 v50, v50, s39, v162
	v_mul_f32_e32 v46, v46, v70
	v_mfma_f32_16x16x32_bf16 v[2:5], v[66:69], v[94:97], v[2:5]
	v_cvt_pk_fp8_f32 v67, v63, 0
	v_mul_f32_e32 v63, v64, v72
	v_med3_f32 v63, v63, s39, v162
	v_cvt_pk_fp8_f32 v64, v63, 0
	s_waitcnt lgkmcnt(0)
	v_mul_f32_e32 v63, v65, v0
	v_med3_f32 v63, v63, s39, v162
	v_cvt_pk_fp8_f32 v65, v63, 0
	v_cvt_pk_fp8_f32 v63, v58, 0
	v_mul_f32_e32 v58, v59, v71
	v_med3_f32 v58, v58, s39, v162
	v_cvt_pk_fp8_f32 v59, v58, 0
	v_mul_f32_e32 v58, v60, v72
	v_med3_f32 v58, v58, s39, v162
	v_cvt_pk_fp8_f32 v60, v58, 0
	v_mul_f32_e32 v58, v61, v0
	v_med3_f32 v58, v58, s39, v162
	v_cvt_pk_fp8_f32 v61, v58, 0
	v_cvt_pk_fp8_f32 v58, v54, 0
	v_mul_f32_e32 v54, v55, v71
	v_med3_f32 v54, v54, s39, v162
	v_cvt_pk_fp8_f32 v55, v54, 0
	v_mul_f32_e32 v54, v56, v72
	v_med3_f32 v54, v54, s39, v162
	v_cvt_pk_fp8_f32 v56, v54, 0
	v_mul_f32_e32 v54, v57, v0
	v_med3_f32 v54, v54, s39, v162
	v_cvt_pk_fp8_f32 v57, v54, 0
	v_cvt_pk_fp8_f32 v54, v50, 0
	v_mul_f32_e32 v50, v51, v71
	v_med3_f32 v50, v50, s39, v162
	v_cvt_pk_fp8_f32 v51, v50, 0
	v_mul_f32_e32 v50, v52, v72
	v_med3_f32 v50, v50, s39, v162
	v_cvt_pk_fp8_f32 v52, v50, 0
	v_mul_f32_e32 v50, v53, v0
	v_med3_f32 v50, v50, s39, v162
	v_cvt_pk_fp8_f32 v53, v50, 0
	v_med3_f32 v46, v46, s39, v162
	v_cvt_pk_fp8_f32 v50, v46, 0
	v_mul_f32_e32 v46, v47, v71
	v_med3_f32 v46, v46, s39, v162
	v_cvt_pk_fp8_f32 v47, v46, 0
	v_mul_f32_e32 v46, v48, v72
	v_med3_f32 v46, v46, s39, v162
	v_cvt_pk_fp8_f32 v48, v46, 0
	v_mul_f32_e32 v46, v49, v0
	v_med3_f32 v46, v46, s39, v162
	v_mul_f32_e32 v42, v42, v70
	v_cvt_pk_fp8_f32 v49, v46, 0
	v_med3_f32 v42, v42, s39, v162
	v_cvt_pk_fp8_f32 v46, v42, 0
	v_mul_f32_e32 v42, v43, v71
	v_med3_f32 v42, v42, s39, v162
	v_cvt_pk_fp8_f32 v43, v42, 0
	v_mul_f32_e32 v42, v44, v72
	v_med3_f32 v42, v42, s39, v162
	v_cvt_pk_fp8_f32 v44, v42, 0
	v_mul_f32_e32 v42, v45, v0
	v_med3_f32 v42, v42, s39, v162
	v_mul_f32_e32 v38, v38, v70
	v_cvt_pk_fp8_f32 v45, v42, 0
	v_med3_f32 v38, v38, s39, v162
	v_cvt_pk_fp8_f32 v42, v38, 0
	v_mul_f32_e32 v38, v39, v71
	v_med3_f32 v38, v38, s39, v162
	v_cvt_pk_fp8_f32 v39, v38, 0
	v_mul_f32_e32 v38, v40, v72
	v_med3_f32 v38, v38, s39, v162
	v_cvt_pk_fp8_f32 v40, v38, 0
	v_mul_f32_e32 v38, v41, v0
	v_med3_f32 v38, v38, s39, v162
	v_mul_f32_e32 v34, v34, v70
	v_cvt_pk_fp8_f32 v41, v38, 0
	v_med3_f32 v34, v34, s39, v162
	v_cvt_pk_fp8_f32 v38, v34, 0
	v_mul_f32_e32 v34, v35, v71
	v_med3_f32 v34, v34, s39, v162
	v_cvt_pk_fp8_f32 v35, v34, 0
	v_mul_f32_e32 v34, v36, v72
	v_med3_f32 v34, v34, s39, v162
	v_cvt_pk_fp8_f32 v36, v34, 0
	v_mul_f32_e32 v34, v37, v0
	v_med3_f32 v34, v34, s39, v162
	v_mul_f32_e32 v30, v30, v70
	v_cvt_pk_fp8_f32 v37, v34, 0
	v_med3_f32 v30, v30, s39, v162
	v_cvt_pk_fp8_f32 v34, v30, 0
	v_mul_f32_e32 v30, v31, v71
	v_med3_f32 v30, v30, s39, v162
	v_cvt_pk_fp8_f32 v31, v30, 0
	v_mul_f32_e32 v30, v32, v72
	v_med3_f32 v30, v30, s39, v162
	v_cvt_pk_fp8_f32 v32, v30, 0
	v_mul_f32_e32 v30, v33, v0
	v_med3_f32 v30, v30, s39, v162
	v_mul_f32_e32 v26, v26, v70
	v_cvt_pk_fp8_f32 v33, v30, 0
	v_med3_f32 v26, v26, s39, v162
	v_cvt_pk_fp8_f32 v30, v26, 0
	v_mul_f32_e32 v26, v27, v71
	v_med3_f32 v26, v26, s39, v162
	v_cvt_pk_fp8_f32 v27, v26, 0
	v_mul_f32_e32 v26, v28, v72
	v_med3_f32 v26, v26, s39, v162
	v_cvt_pk_fp8_f32 v28, v26, 0
	v_mul_f32_e32 v26, v29, v0
	v_med3_f32 v26, v26, s39, v162
	v_mul_f32_e32 v22, v22, v70
	v_cvt_pk_fp8_f32 v29, v26, 0
	v_med3_f32 v22, v22, s39, v162
	v_cvt_pk_fp8_f32 v26, v22, 0
	v_mul_f32_e32 v22, v23, v71
	v_med3_f32 v22, v22, s39, v162
	v_cvt_pk_fp8_f32 v23, v22, 0
	v_mul_f32_e32 v22, v24, v72
	v_med3_f32 v22, v22, s39, v162
	v_cvt_pk_fp8_f32 v24, v22, 0
	v_mul_f32_e32 v22, v25, v0
	v_med3_f32 v22, v22, s39, v162
	v_mul_f32_e32 v18, v18, v70
	v_cvt_pk_fp8_f32 v25, v22, 0
	v_med3_f32 v18, v18, s39, v162
	v_cvt_pk_fp8_f32 v22, v18, 0
	v_mul_f32_e32 v18, v19, v71
	v_med3_f32 v18, v18, s39, v162
	v_cvt_pk_fp8_f32 v19, v18, 0
	v_mul_f32_e32 v18, v20, v72
	v_med3_f32 v18, v18, s39, v162
	v_cvt_pk_fp8_f32 v20, v18, 0
	v_mul_f32_e32 v18, v21, v0
	v_med3_f32 v18, v18, s39, v162
	v_mul_f32_e32 v14, v14, v70
	v_cvt_pk_fp8_f32 v21, v18, 0
	v_med3_f32 v14, v14, s39, v162
	v_cvt_pk_fp8_f32 v18, v14, 0
	v_mul_f32_e32 v14, v15, v71
	v_med3_f32 v14, v14, s39, v162
	v_cvt_pk_fp8_f32 v15, v14, 0
	v_mul_f32_e32 v14, v16, v72
	v_med3_f32 v14, v14, s39, v162
	v_cvt_pk_fp8_f32 v16, v14, 0
	v_mul_f32_e32 v14, v17, v0
	v_med3_f32 v14, v14, s39, v162
	v_mul_f32_e32 v10, v10, v70
	v_cvt_pk_fp8_f32 v17, v14, 0
	v_med3_f32 v10, v10, s39, v162
	v_cvt_pk_fp8_f32 v14, v10, 0
	v_mul_f32_e32 v10, v11, v71
	v_med3_f32 v10, v10, s39, v162
	v_cvt_pk_fp8_f32 v11, v10, 0
	v_mul_f32_e32 v10, v12, v72
	v_med3_f32 v10, v10, s39, v162
	v_cvt_pk_fp8_f32 v12, v10, 0
	v_mul_f32_e32 v10, v13, v0
	v_med3_f32 v10, v10, s39, v162
	v_mul_f32_e32 v6, v6, v70
	v_cvt_pk_fp8_f32 v13, v10, 0
	v_med3_f32 v6, v6, s39, v162
	v_cvt_pk_fp8_f32 v10, v6, 0
	v_mul_f32_e32 v6, v7, v71
	v_med3_f32 v6, v6, s39, v162
	v_cvt_pk_fp8_f32 v7, v6, 0
	v_mul_f32_e32 v6, v8, v72
	v_med3_f32 v6, v6, s39, v162
	v_cvt_pk_fp8_f32 v8, v6, 0
	v_mul_f32_e32 v6, v9, v0
	v_med3_f32 v6, v6, s39, v162
	v_mul_f32_e32 v2, v2, v70
	v_cvt_pk_fp8_f32 v9, v6, 0
	v_med3_f32 v2, v2, s39, v162
	v_mul_f32_e32 v62, v62, v70
	v_cvt_pk_fp8_f32 v6, v2, 0
	v_mul_f32_e32 v2, v3, v71
	v_med3_f32 v62, v62, s39, v162
	v_med3_f32 v2, v2, s39, v162
	v_cvt_pk_fp8_f32 v66, v62, 0
	v_cvt_pk_fp8_f32 v3, v2, 0
	v_mul_f32_e32 v2, v4, v72
	v_med3_f32 v2, v2, s39, v162
	v_mul_f32_e32 v0, v5, v0
	v_lshlrev_b32_e32 v62, 10, v164
	v_cvt_pk_fp8_f32 v4, v2, 0
	v_med3_f32 v0, v0, s39, v162
	v_add3_u32 v62, s23, v163, v62
	v_cvt_pk_fp8_f32 v2, v0, 0
	ds_write_b8 v62, v66
	ds_write_b8 v62, v67 offset:256
	ds_write_b8 v62, v64 offset:512
	ds_write_b8 v62, v65 offset:768
	ds_write_b8 v62, v63 offset:16
	ds_write_b8 v62, v59 offset:272
	ds_write_b8 v62, v60 offset:528
	ds_write_b8 v62, v61 offset:784
	ds_write_b8 v62, v58 offset:32
	ds_write_b8 v62, v55 offset:288
	ds_write_b8 v62, v56 offset:544
	ds_write_b8 v62, v57 offset:800
	ds_write_b8 v62, v54 offset:48
	ds_write_b8 v62, v51 offset:304
	ds_write_b8 v62, v52 offset:560
	ds_write_b8 v62, v53 offset:816
	ds_write_b8 v62, v50 offset:64
	ds_write_b8 v62, v47 offset:320
	ds_write_b8 v62, v48 offset:576
	ds_write_b8 v62, v49 offset:832
	ds_write_b8 v62, v46 offset:80
	ds_write_b8 v62, v43 offset:336
	ds_write_b8 v62, v44 offset:592
	ds_write_b8 v62, v45 offset:848
	ds_write_b8 v62, v42 offset:96
	ds_write_b8 v62, v39 offset:352
	ds_write_b8 v62, v40 offset:608
	ds_write_b8 v62, v41 offset:864
	ds_write_b8 v62, v38 offset:112
	ds_write_b8 v62, v35 offset:368
	ds_write_b8 v62, v36 offset:624
	ds_write_b8 v62, v37 offset:880
	ds_write_b8 v62, v34 offset:128
	ds_write_b8 v62, v31 offset:384
	ds_write_b8 v62, v32 offset:640
	ds_write_b8 v62, v33 offset:896
	ds_write_b8 v62, v30 offset:144
	ds_write_b8 v62, v27 offset:400
	ds_write_b8 v62, v28 offset:656
	ds_write_b8 v62, v29 offset:912
	ds_write_b8 v62, v26 offset:160
	ds_write_b8 v62, v23 offset:416
	ds_write_b8 v62, v24 offset:672
	ds_write_b8 v62, v25 offset:928
	ds_write_b8 v62, v22 offset:176
	ds_write_b8 v62, v19 offset:432
	ds_write_b8 v62, v20 offset:688
	ds_write_b8 v62, v21 offset:944
	ds_write_b8 v62, v18 offset:192
	ds_write_b8 v62, v15 offset:448
	ds_write_b8 v62, v16 offset:704
	ds_write_b8 v62, v17 offset:960
	ds_write_b8 v62, v14 offset:208
	ds_write_b8 v62, v11 offset:464
	ds_write_b8 v62, v12 offset:720
	ds_write_b8 v62, v13 offset:976
	ds_write_b8 v62, v10 offset:224
	ds_write_b8 v62, v7 offset:480
	ds_write_b8 v62, v8 offset:736
	ds_write_b8 v62, v9 offset:992
	ds_write_b8 v62, v6 offset:240
	ds_write_b8 v62, v3 offset:496
	ds_write_b8 v62, v4 offset:752
	ds_write_b8 v62, v2 offset:1008
	s_waitcnt lgkmcnt(0)
	v_lshl_add_u32 v0, v154, 4, s23
	ds_read_b128 v[2:5], v0
	ds_read_b128 v[6:9], v0 offset:1024
	ds_read_b128 v[10:13], v0 offset:2048
	ds_read_b128 v[14:17], v0 offset:3072
	v_lshl_add_u64 v[18:19], v[154:155], 4, s[2:3]
	s_waitcnt lgkmcnt(3)
	global_store_dwordx4 v[18:19], v[2:5], off nt
	s_waitcnt lgkmcnt(2)
	global_store_dwordx4 v[18:19], v[6:9], off offset:1024 nt
	s_waitcnt lgkmcnt(1)
	global_store_dwordx4 v[18:19], v[10:13], off offset:2048 nt
	s_waitcnt lgkmcnt(0)
	global_store_dwordx4 v[18:19], v[14:17], off offset:3072 nt
	s_waitcnt lgkmcnt(0)
	s_branch .LBB0_1473
